# gate K-loop: the redundant next-tile staging loads of a tile's last K iteration run with one active lane (single-tile units have no successor to prefetch)
# baseline (speedup 1.0000x reference)
; #define G8_STAGE(bufoff, gbase, voff) do { _Pragma("unroll") for (int _i = 0; _i < 2; ++_i) \
;         __builtin_amdgcn_global_load_lds((const unsigned*)((const char*)(gbase) + (voff)[_i]), (LAS unsigned*)(lds + (bufoff) + ldsw + _i * 8192), 16, 0, 0); } while (0)
; #define G8_STAGE_A(bufoff, gbase, h_, nx_) do { if constexpr (Sched::GATHER) { unsigned vo_[2]; _Pragma("unroll") for (int q_ = 0; q_ < 2; ++q_) vo_[q_] = (nx_) ? gnxt[h_][q_] : goff[h_][q_]; G8_STAGE(bufoff, gbase, vo_); } \
;         else { G8_STAGE(bufoff, (gbase) + ((h_) ? hstepA : (size_t)0), voffA); } } while (0)
; #define G8_XLDA(b, h) do { if constexpr (Epi::FP8) { G8_LD8(A8, G8_SA(b, h) + aoff, 4); } else { G8_LDA(At, b, h); } } while (0)
; #define G8_XLDB0(b, h) do { if constexpr (Epi::FP8) { G8_LD8(B08, G8_SB(b, h) + boff, 2); } else { G8_LDB(B0, b, h); } } while (0)
; #define G8_XLDB1(b, h) do { if constexpr (Epi::FP8) { G8_LD8(B18, G8_SB(b, h) + boff, 2); } else { G8_LDB(B1, b, h); } } while (0)
; #define G8_MM0(ai, bj) do { if constexpr (Epi::FP8) { G8_MMA8(ai, bj, A8, B08); } else { G8_MMA(ai, bj, At, B0); } } while (0)
; #define G8_MM1(ai, bj) do { if constexpr (Epi::FP8) { G8_MMA8(ai, bj, A8, B18); } else { G8_MMA(ai, bj, At, B1); } } while (0)
; template <int lda, int ldb, class Epi, class Sched>
; __device__ __forceinline__ void gemm_phase(LAS unsigned char* lds, int wid, int lane, const char* baseA, const char* baseB, const Sched& S, const Epi& E) {
;     ...
;         for (int t = 0; t < nt; t += 2) {
;             const bool last = (t == nt - 2);
;             const char* a1 = cA + (size_t)(t + 1) * kstep;
;             const char* a2 = last ? nA : cA + (size_t)(t + 2) * kstep; const char* b2 = last ? nB : cB + (size_t)(t + 2) * kstep;
;             const char* a3 = a2 + kstep; const char* b3 = b2 + kstep;
;     ...
;             G8_XLDB0(0, 0); if constexpr (!Epi::HALFN) { G8_XLDB1(0, 1); } G8_SCHED; G8_XLDA(0, 0); G8_STAGE_A(G8_SA(1, 1), a1, 1, false);
;             G8_WAIT_VK; G8_WAIT_L(0); G8_BAR; G8_MM0(0, 0); if constexpr (!Epi::HALFN) { G8_MM1(0, 1); } G8_BAR; G8_SCHED;
;             G8_XLDA(0, 1); G8_STAGE(G8_SB(0, 0), b2, voffB); if constexpr (!Epi::HALFN) { G8_STAGE(G8_SB(0, 1), b2 + hstepB, voffB); } G8_STAGE_A(G8_SA(0, 0), a2, 0, last);
;             G8_WAIT_VK; G8_WAIT_L(0); G8_BAR; G8_MM0(1, 0); if constexpr (!Epi::HALFN) { G8_MM1(1, 1); } G8_BAR; G8_SCHED;
.LBB0_1085:
	ds_read_b128 v[4:7], v177
	ds_read_b128 v[8:11], v178
	ds_read_b128 v[0:3], v30
	ds_read_b128 v[184:187], v148
	ds_read_b128 v[12:15], v179
	ds_read_b128 v[188:191], v180
	ds_read_b128 v[192:195], v181
	ds_read_b128 v[196:199], v205
	s_add_i32 s83, s54, 2
	s_add_u32 s55, s52, 0xfffe0080
	s_addc_u32 s56, s53, -1
	s_cmp_eq_u32 s80, s54
	s_cselect_b32 s54, s79, s81
	s_cselect_b32 s57, s21, s56
	s_cselect_b32 s56, s28, s55
	s_cselect_b32 s55, s29, s82
	s_cselect_b64 vcc, s[16:17], -1
	s_or_b64 vcc, vcc, 1
	v_lshl_add_u64 v[152:153], s[52:53], 0, v[166:167]
	s_add_i32 m0, s27, 0xc000
	ds_read_b128 v[168:171], v212
	ds_read_b128 v[172:175], v212 offset:1024
	ds_read_b128 v[214:217], v212 offset:2048
	ds_read_b128 v[218:221], v212 offset:3072
	ds_read_b128 v[222:225], v212 offset:4096
	ds_read_b128 v[226:229], v212 offset:5120
	ds_read_b128 v[230:233], v212 offset:6144
	ds_read_b128 v[234:237], v212 offset:7168
	global_load_lds_dwordx4 v[152:153], off
	v_lshl_add_u64 v[152:153], s[52:53], 0, v[164:165]
	s_add_i32 m0, s27, 0xe000
	s_nop 0
	global_load_lds_dwordx4 v[152:153], off
	s_waitcnt vmcnt(8)
	s_waitcnt lgkmcnt(0)
	s_barrier
	s_setprio 1
	s_waitcnt lgkmcnt(0)
	v_mfma_scale_f32_16x16x128_f8f6f4 v[144:147], v[0:7], v[168:175], v[144:147], v213, v213 op_sel_hi:[0,0,0]
	v_mfma_scale_f32_16x16x128_f8f6f4 v[140:143], v[8:15], v[168:175], v[140:143], v213, v213 op_sel_hi:[0,0,0]
	v_mfma_scale_f32_16x16x128_f8f6f4 v[136:139], v[0:7], v[214:221], v[136:139], v213, v213 op_sel_hi:[0,0,0]
	v_mfma_scale_f32_16x16x128_f8f6f4 v[132:135], v[8:15], v[214:221], v[132:135], v213, v213 op_sel_hi:[0,0,0]
	v_mfma_scale_f32_16x16x128_f8f6f4 v[128:131], v[0:7], v[222:229], v[128:131], v213, v213 op_sel_hi:[0,0,0]
	v_mfma_scale_f32_16x16x128_f8f6f4 v[124:127], v[8:15], v[222:229], v[124:127], v213, v213 op_sel_hi:[0,0,0]
	v_mfma_scale_f32_16x16x128_f8f6f4 v[120:123], v[0:7], v[230:237], v[120:123], v213, v213 op_sel_hi:[0,0,0]
	v_mfma_scale_f32_16x16x128_f8f6f4 v[116:119], v[8:15], v[230:237], v[116:119], v213, v213 op_sel_hi:[0,0,0]
	s_setprio 0
	s_setprio 1
	v_mfma_scale_f32_16x16x128_f8f6f4 v[80:83], v[184:191], v[168:175], v[80:83], v213, v213 op_sel_hi:[0,0,0]
	v_mfma_scale_f32_16x16x128_f8f6f4 v[76:79], v[192:199], v[168:175], v[76:79], v213, v213 op_sel_hi:[0,0,0]
	v_mfma_scale_f32_16x16x128_f8f6f4 v[72:75], v[184:191], v[214:221], v[72:75], v213, v213 op_sel_hi:[0,0,0]
	v_mfma_scale_f32_16x16x128_f8f6f4 v[68:71], v[192:199], v[214:221], v[68:71], v213, v213 op_sel_hi:[0,0,0]
	v_mfma_scale_f32_16x16x128_f8f6f4 v[64:67], v[184:191], v[222:229], v[64:67], v213, v213 op_sel_hi:[0,0,0]
	v_mfma_scale_f32_16x16x128_f8f6f4 v[60:63], v[192:199], v[222:229], v[60:63], v213, v213 op_sel_hi:[0,0,0]
	v_mfma_scale_f32_16x16x128_f8f6f4 v[56:59], v[184:191], v[230:237], v[56:59], v213, v213 op_sel_hi:[0,0,0]
	v_mfma_scale_f32_16x16x128_f8f6f4 v[52:55], v[192:199], v[230:237], v[52:55], v213, v213 op_sel_hi:[0,0,0]
	s_setprio 0
	s_barrier
	s_mov_b32 m0, s60
	v_lshl_add_u64 v[168:169], s[54:55], 0, v[160:161]
	s_add_u32 s84, s54, 0x20000
	ds_read_b128 v[214:217], v212 offset:16384
	ds_read_b128 v[218:221], v212 offset:17408
	ds_read_b128 v[222:225], v212 offset:18432
	ds_read_b128 v[226:229], v212 offset:19456
	ds_read_b128 v[230:233], v212 offset:20480
	ds_read_b128 v[234:237], v212 offset:21504
	ds_read_b128 v[238:241], v212 offset:22528
	ds_read_b128 v[242:245], v212 offset:23552
	s_mov_b64 exec, vcc
	global_load_lds_dwordx4 v[168:169], off
	s_mov_b64 exec, -1
	v_lshl_add_u64 v[170:171], s[54:55], 0, v[156:157]
	s_mov_b32 m0, s61
	s_addc_u32 s85, s55, 0
	s_mov_b64 exec, vcc
	global_load_lds_dwordx4 v[170:171], off
	s_mov_b64 exec, -1
	v_lshl_add_u64 v[152:153], s[84:85], 0, v[160:161]
	s_mov_b32 m0, s62
	v_lshl_add_u64 v[172:173], s[56:57], 0, v[162:163]
	s_mov_b64 exec, vcc
	global_load_lds_dwordx4 v[152:153], off
	s_mov_b64 exec, -1
	v_lshl_add_u64 v[152:153], s[84:85], 0, v[156:157]
	s_mov_b32 m0, s63
	v_lshl_add_u64 v[174:175], s[56:57], 0, v[158:159]
	s_mov_b64 exec, vcc
	global_load_lds_dwordx4 v[152:153], off
	s_mov_b64 exec, -1
	s_mov_b32 m0, s27
	s_nop 0
	s_mov_b64 exec, vcc
	global_load_lds_dwordx4 v[172:173], off
	s_mov_b64 exec, -1
	s_mov_b32 m0, s64
	s_nop 0
	s_mov_b64 exec, vcc
	global_load_lds_dwordx4 v[174:175], off
	s_mov_b64 exec, -1
	s_waitcnt vmcnt(8)
	s_waitcnt lgkmcnt(0)
	s_barrier
	s_setprio 1
	s_waitcnt lgkmcnt(0)
	v_mfma_scale_f32_16x16x128_f8f6f4 v[112:115], v[0:7], v[214:221], v[112:115], v213, v213 op_sel_hi:[0,0,0]
	v_mfma_scale_f32_16x16x128_f8f6f4 v[108:111], v[8:15], v[214:221], v[108:111], v213, v213 op_sel_hi:[0,0,0]
	v_mfma_scale_f32_16x16x128_f8f6f4 v[104:107], v[0:7], v[222:229], v[104:107], v213, v213 op_sel_hi:[0,0,0]
	v_mfma_scale_f32_16x16x128_f8f6f4 v[100:103], v[8:15], v[222:229], v[100:103], v213, v213 op_sel_hi:[0,0,0]
	v_mfma_scale_f32_16x16x128_f8f6f4 v[96:99], v[0:7], v[230:237], v[96:99], v213, v213 op_sel_hi:[0,0,0]
	v_mfma_scale_f32_16x16x128_f8f6f4 v[92:95], v[8:15], v[230:237], v[92:95], v213, v213 op_sel_hi:[0,0,0]
	v_mfma_scale_f32_16x16x128_f8f6f4 v[88:91], v[0:7], v[238:245], v[88:91], v213, v213 op_sel_hi:[0,0,0]
	v_mfma_scale_f32_16x16x128_f8f6f4 v[84:87], v[8:15], v[238:245], v[84:87], v213, v213 op_sel_hi:[0,0,0]
	s_setprio 0
	s_setprio 1
	v_mfma_scale_f32_16x16x128_f8f6f4 v[48:51], v[184:191], v[214:221], v[48:51], v213, v213 op_sel_hi:[0,0,0]
	v_mfma_scale_f32_16x16x128_f8f6f4 v[44:47], v[192:199], v[214:221], v[44:47], v213, v213 op_sel_hi:[0,0,0]
	v_mfma_scale_f32_16x16x128_f8f6f4 v[40:43], v[184:191], v[222:229], v[40:43], v213, v213 op_sel_hi:[0,0,0]
	v_mfma_scale_f32_16x16x128_f8f6f4 v[36:39], v[192:199], v[222:229], v[36:39], v213, v213 op_sel_hi:[0,0,0]
	v_mfma_scale_f32_16x16x128_f8f6f4 v[32:35], v[184:191], v[230:237], v[32:35], v213, v213 op_sel_hi:[0,0,0]
	v_mfma_scale_f32_16x16x128_f8f6f4 v[26:29], v[192:199], v[230:237], v[26:29], v213, v213 op_sel_hi:[0,0,0]
	v_mfma_scale_f32_16x16x128_f8f6f4 v[22:25], v[184:191], v[238:245], v[22:25], v213, v213 op_sel_hi:[0,0,0]
	v_mfma_scale_f32_16x16x128_f8f6f4 v[18:21], v[192:199], v[238:245], v[18:21], v213, v213 op_sel_hi:[0,0,0]
	s_setprio 0
	s_barrier
; #define G8_STAGE(bufoff, gbase, voff) do { _Pragma("unroll") for (int _i = 0; _i < 2; ++_i) \
;         __builtin_amdgcn_global_load_lds((const unsigned*)((const char*)(gbase) + (voff)[_i]), (LAS unsigned*)(lds + (bufoff) + ldsw + _i * 8192), 16, 0, 0); } while (0)
; #define G8_STAGE_A(bufoff, gbase, h_, nx_) do { if constexpr (Sched::GATHER) { unsigned vo_[2]; _Pragma("unroll") for (int q_ = 0; q_ < 2; ++q_) vo_[q_] = (nx_) ? gnxt[h_][q_] : goff[h_][q_]; G8_STAGE(bufoff, gbase, vo_); } \
;         else { G8_STAGE(bufoff, (gbase) + ((h_) ? hstepA : (size_t)0), voffA); } } while (0)
; #define G8_XLDA(b, h) do { if constexpr (Epi::FP8) { G8_LD8(A8, G8_SA(b, h) + aoff, 4); } else { G8_LDA(At, b, h); } } while (0)
; #define G8_XLDB0(b, h) do { if constexpr (Epi::FP8) { G8_LD8(B08, G8_SB(b, h) + boff, 2); } else { G8_LDB(B0, b, h); } } while (0)
; #define G8_XLDB1(b, h) do { if constexpr (Epi::FP8) { G8_LD8(B18, G8_SB(b, h) + boff, 2); } else { G8_LDB(B1, b, h); } } while (0)
; #define G8_MM0(ai, bj) do { if constexpr (Epi::FP8) { G8_MMA8(ai, bj, A8, B08); } else { G8_MMA(ai, bj, At, B0); } } while (0)
; #define G8_MM1(ai, bj) do { if constexpr (Epi::FP8) { G8_MMA8(ai, bj, A8, B18); } else { G8_MMA(ai, bj, At, B1); } } while (0)
; #define G8_WAIT_L(n) asm volatile("s_waitcnt lgkmcnt(" #n ")" ::: "memory")
; #define G8_BAR __builtin_amdgcn_s_barrier()
; #define G8_SCHED __builtin_amdgcn_sched_barrier(0)
; #define G8_WAIT_VK do { if constexpr (Epi::HALFN) { G8_WAIT_V(6); } else { G8_WAIT_V(8); } } while (0)
; template <int lda, int ldb, class Epi, class Sched>
; __device__ __forceinline__ void gemm_phase(LAS unsigned char* lds, int wid, int lane, const char* baseA, const char* baseB, const Sched& S, const Epi& E) {
;     ...
;             G8_XLDB0(1, 0); if constexpr (!Epi::HALFN) { G8_XLDB1(1, 1); } G8_SCHED; G8_XLDA(1, 0); G8_STAGE_A(G8_SA(0, 1), a2, 1, last);
;             G8_WAIT_VK; G8_WAIT_L(0); G8_BAR; G8_MM0(0, 0); if constexpr (!Epi::HALFN) { G8_MM1(0, 1); } G8_BAR; G8_SCHED;
;             G8_XLDA(1, 1); G8_STAGE(G8_SB(1, 0), b3, voffB); if constexpr (!Epi::HALFN) { G8_STAGE(G8_SB(1, 1), b3 + hstepB, voffB); } G8_STAGE_A(G8_SA(1, 0), a3, 0, last);
;             G8_WAIT_VK; G8_WAIT_L(0); G8_BAR; G8_MM0(1, 0); if constexpr (!Epi::HALFN) { G8_MM1(1, 1); } G8_BAR; G8_SCHED;
;         }
	ds_read_b128 v[12:15], v206
	ds_read_b128 v[184:187], v207
	ds_read_b128 v[8:11], v151
	ds_read_b128 v[0:3], v176
	ds_read_b128 v[188:191], v208
	ds_read_b128 v[4:7], v209
	ds_read_b128 v[192:195], v210
	ds_read_b128 v[196:199], v211
	s_add_u32 s56, s56, 0x20000
	s_addc_u32 s57, s57, 0
	s_mov_b32 m0, s65
	v_lshl_add_u64 v[152:153], s[56:57], 0, v[162:163]
	ds_read_b128 v[214:217], v212 offset:32768
	ds_read_b128 v[218:221], v212 offset:33792
	ds_read_b128 v[222:225], v212 offset:34816
	ds_read_b128 v[226:229], v212 offset:35840
	ds_read_b128 v[230:233], v212 offset:36864
	ds_read_b128 v[234:237], v212 offset:37888
	ds_read_b128 v[238:241], v212 offset:38912
	ds_read_b128 v[242:245], v212 offset:39936
	s_mov_b64 exec, vcc
	global_load_lds_dwordx4 v[152:153], off
	s_mov_b64 exec, -1
	v_lshl_add_u64 v[152:153], s[56:57], 0, v[158:159]
	s_mov_b32 m0, s66
	s_nop 0
	s_mov_b64 exec, vcc
	global_load_lds_dwordx4 v[152:153], off
	s_mov_b64 exec, -1
	s_waitcnt vmcnt(8)
	s_waitcnt lgkmcnt(0)
	s_barrier
	s_setprio 1
	s_waitcnt lgkmcnt(0)
	v_mfma_scale_f32_16x16x128_f8f6f4 v[144:147], v[8:15], v[214:221], v[144:147], v213, v213 op_sel_hi:[0,0,0]
	v_mfma_scale_f32_16x16x128_f8f6f4 v[140:143], v[184:191], v[214:221], v[140:143], v213, v213 op_sel_hi:[0,0,0]
	v_mfma_scale_f32_16x16x128_f8f6f4 v[136:139], v[8:15], v[222:229], v[136:139], v213, v213 op_sel_hi:[0,0,0]
	v_mfma_scale_f32_16x16x128_f8f6f4 v[132:135], v[184:191], v[222:229], v[132:135], v213, v213 op_sel_hi:[0,0,0]
	v_mfma_scale_f32_16x16x128_f8f6f4 v[128:131], v[8:15], v[230:237], v[128:131], v213, v213 op_sel_hi:[0,0,0]
	v_mfma_scale_f32_16x16x128_f8f6f4 v[124:127], v[184:191], v[230:237], v[124:127], v213, v213 op_sel_hi:[0,0,0]
	v_mfma_scale_f32_16x16x128_f8f6f4 v[120:123], v[8:15], v[238:245], v[120:123], v213, v213 op_sel_hi:[0,0,0]
	v_mfma_scale_f32_16x16x128_f8f6f4 v[116:119], v[184:191], v[238:245], v[116:119], v213, v213 op_sel_hi:[0,0,0]
	s_setprio 0
	s_setprio 1
	v_mfma_scale_f32_16x16x128_f8f6f4 v[80:83], v[0:7], v[214:221], v[80:83], v213, v213 op_sel_hi:[0,0,0]
	v_mfma_scale_f32_16x16x128_f8f6f4 v[76:79], v[192:199], v[214:221], v[76:79], v213, v213 op_sel_hi:[0,0,0]
	v_mfma_scale_f32_16x16x128_f8f6f4 v[72:75], v[0:7], v[222:229], v[72:75], v213, v213 op_sel_hi:[0,0,0]
	v_mfma_scale_f32_16x16x128_f8f6f4 v[68:71], v[192:199], v[222:229], v[68:71], v213, v213 op_sel_hi:[0,0,0]
	v_mfma_scale_f32_16x16x128_f8f6f4 v[64:67], v[0:7], v[230:237], v[64:67], v213, v213 op_sel_hi:[0,0,0]
	v_mfma_scale_f32_16x16x128_f8f6f4 v[60:63], v[192:199], v[230:237], v[60:63], v213, v213 op_sel_hi:[0,0,0]
	v_mfma_scale_f32_16x16x128_f8f6f4 v[56:59], v[0:7], v[238:245], v[56:59], v213, v213 op_sel_hi:[0,0,0]
	v_mfma_scale_f32_16x16x128_f8f6f4 v[52:55], v[192:199], v[238:245], v[52:55], v213, v213 op_sel_hi:[0,0,0]
	s_setprio 0
	s_barrier
	s_mov_b32 m0, s67
	v_lshl_add_u64 v[152:153], v[168:169], 0, s[22:23]
	s_add_u32 s54, s54, 0x20080
	ds_read_b128 v[214:217], v212 offset:49152
	ds_read_b128 v[218:221], v212 offset:50176
	ds_read_b128 v[222:225], v212 offset:51200
	ds_read_b128 v[226:229], v212 offset:52224
	ds_read_b128 v[230:233], v212 offset:53248
	ds_read_b128 v[234:237], v212 offset:54272
	ds_read_b128 v[238:241], v212 offset:55296
	ds_read_b128 v[242:245], v212 offset:56320
	s_mov_b64 exec, vcc
	global_load_lds_dwordx4 v[152:153], off
	s_mov_b64 exec, -1
	v_lshl_add_u64 v[152:153], v[170:171], 0, s[22:23]
	s_mov_b32 m0, s68
	s_addc_u32 s55, s55, 0
	s_mov_b64 exec, vcc
	global_load_lds_dwordx4 v[152:153], off
	s_mov_b64 exec, -1
	v_lshl_add_u64 v[152:153], s[54:55], 0, v[160:161]
	s_mov_b32 m0, s71
	s_nop 0
	s_mov_b64 exec, vcc
	global_load_lds_dwordx4 v[152:153], off
	s_mov_b64 exec, -1
	v_lshl_add_u64 v[152:153], s[54:55], 0, v[156:157]
	s_mov_b32 m0, s72
	s_nop 0
	s_mov_b64 exec, vcc
	global_load_lds_dwordx4 v[152:153], off
	s_mov_b64 exec, -1
	v_lshl_add_u64 v[152:153], v[172:173], 0, s[22:23]
	s_mov_b32 m0, s69
	s_nop 0
	s_mov_b64 exec, vcc
	global_load_lds_dwordx4 v[152:153], off
	s_mov_b64 exec, -1
	v_lshl_add_u64 v[152:153], v[174:175], 0, s[22:23]
	s_mov_b32 m0, s70
	s_nop 0
	s_mov_b64 exec, vcc
	global_load_lds_dwordx4 v[152:153], off
	s_mov_b64 exec, -1
	s_waitcnt vmcnt(8)
	s_waitcnt lgkmcnt(0)
	s_barrier
	s_setprio 1
	s_waitcnt lgkmcnt(0)
	v_mfma_scale_f32_16x16x128_f8f6f4 v[112:115], v[8:15], v[214:221], v[112:115], v213, v213 op_sel_hi:[0,0,0]
	v_mfma_scale_f32_16x16x128_f8f6f4 v[108:111], v[184:191], v[214:221], v[108:111], v213, v213 op_sel_hi:[0,0,0]
	v_mfma_scale_f32_16x16x128_f8f6f4 v[104:107], v[8:15], v[222:229], v[104:107], v213, v213 op_sel_hi:[0,0,0]
	v_mfma_scale_f32_16x16x128_f8f6f4 v[100:103], v[184:191], v[222:229], v[100:103], v213, v213 op_sel_hi:[0,0,0]
	v_mfma_scale_f32_16x16x128_f8f6f4 v[96:99], v[8:15], v[230:237], v[96:99], v213, v213 op_sel_hi:[0,0,0]
	v_mfma_scale_f32_16x16x128_f8f6f4 v[92:95], v[184:191], v[230:237], v[92:95], v213, v213 op_sel_hi:[0,0,0]
	v_mfma_scale_f32_16x16x128_f8f6f4 v[88:91], v[8:15], v[238:245], v[88:91], v213, v213 op_sel_hi:[0,0,0]
	v_mfma_scale_f32_16x16x128_f8f6f4 v[84:87], v[184:191], v[238:245], v[84:87], v213, v213 op_sel_hi:[0,0,0]
	s_setprio 0
	s_setprio 1
	v_mfma_scale_f32_16x16x128_f8f6f4 v[48:51], v[0:7], v[214:221], v[48:51], v213, v213 op_sel_hi:[0,0,0]
	v_mfma_scale_f32_16x16x128_f8f6f4 v[44:47], v[192:199], v[214:221], v[44:47], v213, v213 op_sel_hi:[0,0,0]
	v_mfma_scale_f32_16x16x128_f8f6f4 v[40:43], v[0:7], v[222:229], v[40:43], v213, v213 op_sel_hi:[0,0,0]
	v_mfma_scale_f32_16x16x128_f8f6f4 v[36:39], v[192:199], v[222:229], v[36:39], v213, v213 op_sel_hi:[0,0,0]
	v_mfma_scale_f32_16x16x128_f8f6f4 v[32:35], v[0:7], v[230:237], v[32:35], v213, v213 op_sel_hi:[0,0,0]
	v_mfma_scale_f32_16x16x128_f8f6f4 v[26:29], v[192:199], v[230:237], v[26:29], v213, v213 op_sel_hi:[0,0,0]
	v_mfma_scale_f32_16x16x128_f8f6f4 v[22:25], v[0:7], v[238:245], v[22:25], v213, v213 op_sel_hi:[0,0,0]
	v_mfma_scale_f32_16x16x128_f8f6f4 v[18:21], v[192:199], v[238:245], v[18:21], v213, v213 op_sel_hi:[0,0,0]
	s_setprio 0
	s_barrier
	s_add_u32 s81, s81, 0x100
	s_addc_u32 s82, s82, 0
	s_add_u32 s52, s52, 0x100
	s_addc_u32 s53, s53, 0
	s_cmp_ge_i32 s83, s4
	s_mov_b32 s54, s83
	s_cbranch_scc0 .LBB0_1085
	s_and_b64 vcc, exec, s[36:37]
	s_cbranch_vccz .LBB0_1088
